# half-peel (C=0 first touch, no accumulator zero-fill) also on attn-out, pool-in, pool-out GEMM K-loops
# baseline (speedup 1.0000x reference)
; #define PG8_STAGEA(bufoff, gbase, h) do { if constexpr (GATHER) { PG8_STAGE(bufoff, gbase, vA[h]); } else { PG8_STAGE(bufoff, (gbase) + (h) * hstepA, voffA); } } while (0)
; #define PG8_LDA(dst, b, h) do { _Pragma("unroll") for (int m = 0; m < 4; ++m) _Pragma("unroll") for (int k = 0; k < 2; ++k) dst[m][k] = *(const LAS bf16x8*)(lds + PG8_SA(b, h) + aoff + m * 2048 + k * 1024); } while (0)
; #define PG8_MM(ai, bj, At, Bt) do { if constexpr (Epi::F8MMA) PG8_MMA8(ai, bj, At, Bt##8); else PG8_MMA(ai, bj, At, Bt); } while (0)
; #define PG8_WAIT_V(n) asm volatile("s_waitcnt vmcnt(" #n ")" ::: "memory")
; #define PG8_WAIT_L(n) asm volatile("s_waitcnt lgkmcnt(" #n ")" ::: "memory")
; #define PG8_BAR __builtin_amdgcn_s_barrier()
; #define PG8_SCHED __builtin_amdgcn_sched_barrier(0)
; template <class Epi, class Sched>
; __device__ __forceinline__ void gemm_phase(const int tid, LAS unsigned char* lds, const char* Abase, const int lda, const int ldb, const int K, const Sched& S, const Epi& E) {
;     ...
;             PG8_LDB(B0, 0, 0); PG8_LDB(B1, 0, 1); PG8_SCHED; PG8_LDA(At, 0, 0); PG8_STAGEA(PG8_SA(1, 1), a1, 1);
;             if constexpr (GATHER) { if (last) {
; #pragma unroll
;                 for (int h = 0; h < 2; ++h)
; #pragma unroll
;                     for (int i = 0; i < 2; ++i) vA[h][i] = vAn[h][i]; } }
;             PG8_WAIT_V(8); PG8_WAIT_L(0); PG8_BAR; PG8_MM(0, 0, At, B0); PG8_MM(0, 1, At, B1); PG8_BAR; PG8_SCHED;
;             PG8_LDA(At, 0, 1); PG8_STAGE(PG8_SB(0, 0), b2, voffB); PG8_STAGE(PG8_SB(0, 1), b2 + hstepB, voffB); PG8_STAGEA(PG8_SA(0, 0), a2, 0);
;             PG8_WAIT_V(8); PG8_WAIT_L(0); PG8_BAR; PG8_MM(1, 0, At, B0); PG8_MM(1, 1, At, B1); PG8_BAR; PG8_SCHED;
.LBB0_661:
	s_andn2_b64 vcc, exec, s[46:47]
	s_cbranch_vccnz .LBB0_667
	v_mov_b32_e32 v209, v3
	v_mov_b32_e32 v211, v3
	s_mov_b32 s79, 0
	s_mov_b64 s[2:3], 0x100
	s_waitcnt lgkmcnt(0)
	s_branch .LBB0_665
.Lpeel_ao:
	s_add_i32 s79, s79, 2
	s_and_b64 s[56:57], s[60:61], exec
	s_cselect_b32 s57, 0, s2
	s_cselect_b32 s56, 0, s3
	s_add_u32 s64, s38, s57
	s_addc_u32 s65, s39, s56
	s_add_u32 s62, s54, s2
	s_addc_u32 s63, s55, s3
	s_add_u32 s56, s64, 0x80
	s_addc_u32 s57, s65, 0
	s_waitcnt vmcnt(8)
	s_and_b64 s[60:61], s[60:61], exec
	s_waitcnt lgkmcnt(0)
	s_cselect_b32 s60, s52, s62
	s_cselect_b32 s61, s53, s63
	s_add_u32 s62, s60, 0x80
	s_addc_u32 s63, s61, 0
	s_barrier
	s_setprio 1
	s_waitcnt lgkmcnt(0)
	v_mfma_scale_f32_16x16x128_f8f6f4 v[192:195], v[20:27], v[60:67], 0, v219, v216 op_sel_hi:[0,0,0]
	v_mfma_scale_f32_16x16x128_f8f6f4 v[188:191], v[28:35], v[60:67], 0, v219, v216 op_sel_hi:[0,0,0]
	v_mfma_scale_f32_16x16x128_f8f6f4 v[176:179], v[20:27], v[52:59], 0, v219, v216 op_sel_hi:[0,0,0]
	v_mfma_scale_f32_16x16x128_f8f6f4 v[172:175], v[28:35], v[52:59], 0, v219, v216 op_sel_hi:[0,0,0]
	v_mfma_scale_f32_16x16x128_f8f6f4 v[160:163], v[20:27], v[44:51], 0, v219, v216 op_sel_hi:[0,0,0]
	v_mfma_scale_f32_16x16x128_f8f6f4 v[156:159], v[28:35], v[44:51], 0, v219, v216 op_sel_hi:[0,0,0]
	v_mfma_scale_f32_16x16x128_f8f6f4 v[144:147], v[20:27], v[36:43], 0, v219, v216 op_sel_hi:[0,0,0]
	v_mfma_scale_f32_16x16x128_f8f6f4 v[140:143], v[28:35], v[36:43], 0, v219, v216 op_sel_hi:[0,0,0]
	s_setprio 0
	s_setprio 1
	v_mfma_scale_f32_16x16x128_f8f6f4 v[184:187], v[4:11], v[60:67], 0, v219, v216 op_sel_hi:[0,0,0]
	v_mfma_scale_f32_16x16x128_f8f6f4 v[180:183], v[12:19], v[60:67], 0, v219, v216 op_sel_hi:[0,0,0]
	v_mfma_scale_f32_16x16x128_f8f6f4 v[168:171], v[4:11], v[52:59], 0, v219, v216 op_sel_hi:[0,0,0]
	v_mfma_scale_f32_16x16x128_f8f6f4 v[164:167], v[12:19], v[52:59], 0, v219, v216 op_sel_hi:[0,0,0]
	v_mfma_scale_f32_16x16x128_f8f6f4 v[152:155], v[4:11], v[44:51], 0, v219, v216 op_sel_hi:[0,0,0]
	v_mfma_scale_f32_16x16x128_f8f6f4 v[148:151], v[12:19], v[44:51], 0, v219, v216 op_sel_hi:[0,0,0]
	v_mfma_scale_f32_16x16x128_f8f6f4 v[136:139], v[4:11], v[36:43], 0, v219, v216 op_sel_hi:[0,0,0]
	v_mfma_scale_f32_16x16x128_f8f6f4 v[132:135], v[12:19], v[36:43], 0, v219, v216 op_sel_hi:[0,0,0]
	s_setprio 0
	s_barrier
	s_mov_b32 m0, s10
	v_lshl_add_u64 v[228:229], s[60:61], 0, v[198:199]
	s_add_u32 s82, s60, 0x8000
	ds_read_b128 v[36:39], v245 offset:16384
	ds_read_b128 v[40:43], v245 offset:17408
	ds_read_b128 v[44:47], v245 offset:18432
	ds_read_b128 v[48:51], v245 offset:19456
	ds_read_b128 v[52:55], v245 offset:20480
	ds_read_b128 v[56:59], v245 offset:21504
	ds_read_b128 v[60:63], v245 offset:22528
	ds_read_b128 v[64:67], v245 offset:23552
	global_load_lds_dwordx4 v[228:229], off
	v_lshl_add_u64 v[228:229], s[60:61], 0, v[196:197]
	s_mov_b32 m0, s11
	s_addc_u32 s83, s61, 0
	global_load_lds_dwordx4 v[228:229], off
	v_lshl_add_u64 v[228:229], s[82:83], 0, v[198:199]
	s_mov_b32 m0, s22
	s_nop 0
	global_load_lds_dwordx4 v[228:229], off
	v_lshl_add_u64 v[228:229], s[82:83], 0, v[196:197]
	s_mov_b32 m0, s25
	s_nop 0
	global_load_lds_dwordx4 v[228:229], off
	s_mov_b32 m0, s9
	s_nop 0
	global_load_lds_dwordx4 v200, s[64:65]
	s_mov_b32 m0, s28
	s_nop 0
	global_load_lds_dwordx4 v202, s[64:65]
	s_waitcnt vmcnt(8)
	s_waitcnt lgkmcnt(0)
	s_barrier
	s_setprio 1
	s_waitcnt lgkmcnt(0)
	v_mfma_scale_f32_16x16x128_f8f6f4 v[128:131], v[20:27], v[36:43], 0, v219, v216 op_sel_hi:[0,0,0]
	v_mfma_scale_f32_16x16x128_f8f6f4 v[124:127], v[28:35], v[36:43], 0, v219, v216 op_sel_hi:[0,0,0]
	v_mfma_scale_f32_16x16x128_f8f6f4 v[112:115], v[20:27], v[44:51], 0, v219, v216 op_sel_hi:[0,0,0]
	v_mfma_scale_f32_16x16x128_f8f6f4 v[108:111], v[28:35], v[44:51], 0, v219, v216 op_sel_hi:[0,0,0]
	v_mfma_scale_f32_16x16x128_f8f6f4 v[96:99], v[20:27], v[52:59], 0, v219, v216 op_sel_hi:[0,0,0]
	v_mfma_scale_f32_16x16x128_f8f6f4 v[92:95], v[28:35], v[52:59], 0, v219, v216 op_sel_hi:[0,0,0]
	v_mfma_scale_f32_16x16x128_f8f6f4 v[80:83], v[20:27], v[60:67], 0, v219, v216 op_sel_hi:[0,0,0]
	v_mfma_scale_f32_16x16x128_f8f6f4 v[76:79], v[28:35], v[60:67], 0, v219, v216 op_sel_hi:[0,0,0]
	s_setprio 0
	s_setprio 1
	v_mfma_scale_f32_16x16x128_f8f6f4 v[120:123], v[4:11], v[36:43], 0, v219, v216 op_sel_hi:[0,0,0]
	v_mfma_scale_f32_16x16x128_f8f6f4 v[116:119], v[12:19], v[36:43], 0, v219, v216 op_sel_hi:[0,0,0]
	v_mfma_scale_f32_16x16x128_f8f6f4 v[104:107], v[4:11], v[44:51], 0, v219, v216 op_sel_hi:[0,0,0]
	v_mfma_scale_f32_16x16x128_f8f6f4 v[100:103], v[12:19], v[44:51], 0, v219, v216 op_sel_hi:[0,0,0]
	v_mfma_scale_f32_16x16x128_f8f6f4 v[88:91], v[4:11], v[52:59], 0, v219, v216 op_sel_hi:[0,0,0]
	v_mfma_scale_f32_16x16x128_f8f6f4 v[84:87], v[12:19], v[52:59], 0, v219, v216 op_sel_hi:[0,0,0]
	v_mfma_scale_f32_16x16x128_f8f6f4 v[72:75], v[4:11], v[60:67], 0, v219, v216 op_sel_hi:[0,0,0]
	v_mfma_scale_f32_16x16x128_f8f6f4 v[68:71], v[12:19], v[60:67], 0, v219, v216 op_sel_hi:[0,0,0]
	s_setprio 0
	s_barrier
	s_branch .Lmid_ao

; #define PG8_STAGEA(bufoff, gbase, h) do { if constexpr (GATHER) { PG8_STAGE(bufoff, gbase, vA[h]); } else { PG8_STAGE(bufoff, (gbase) + (h) * hstepA, voffA); } } while (0)
; #define PG8_LDA(dst, b, h) do { _Pragma("unroll") for (int m = 0; m < 4; ++m) _Pragma("unroll") for (int k = 0; k < 2; ++k) dst[m][k] = *(const LAS bf16x8*)(lds + PG8_SA(b, h) + aoff + m * 2048 + k * 1024); } while (0)
; #define PG8_MM(ai, bj, At, Bt) do { if constexpr (Epi::F8MMA) PG8_MMA8(ai, bj, At, Bt##8); else PG8_MMA(ai, bj, At, Bt); } while (0)
; #define PG8_WAIT_V(n) asm volatile("s_waitcnt vmcnt(" #n ")" ::: "memory")
; #define PG8_WAIT_L(n) asm volatile("s_waitcnt lgkmcnt(" #n ")" ::: "memory")
; #define PG8_BAR __builtin_amdgcn_s_barrier()
; #define PG8_SCHED __builtin_amdgcn_sched_barrier(0)
; template <class Epi, class Sched>
; __device__ __forceinline__ void gemm_phase(const int tid, LAS unsigned char* lds, const char* Abase, const int lda, const int ldb, const int K, const Sched& S, const Epi& E) {
;     ...
;             PG8_LDB(B0, 1, 0); PG8_LDB(B1, 1, 1); PG8_SCHED; PG8_LDA(At, 1, 0); PG8_STAGEA(PG8_SA(0, 1), a2, 1);
;             PG8_WAIT_V(8); PG8_WAIT_L(0); PG8_BAR; PG8_MM(0, 0, At, B0); PG8_MM(0, 1, At, B1); PG8_BAR; PG8_SCHED;
;             PG8_LDA(At, 1, 1); PG8_STAGE(PG8_SB(1, 0), b3, voffB); PG8_STAGE(PG8_SB(1, 1), b3 + hstepB, voffB); PG8_STAGEA(PG8_SA(1, 0), a3, 0);
;             PG8_WAIT_V(8); PG8_WAIT_L(0); PG8_BAR; PG8_MM(1, 0, At, B0); PG8_MM(1, 1, At, B1); PG8_BAR; PG8_SCHED;
;         }
.Lmid_ao:
	s_add_i32 s82, 0, 0x18000
	s_add_i32 s83, 0, 0x1c000
	v_add_u32_e32 v16, s82, v201
	v_add_u32_e32 v32, s83, v201
	ds_read_b128 v[4:7], v16
	ds_read_b128 v[8:11], v16 offset:1024
	ds_read_b128 v[12:15], v16 offset:2048
	ds_read_b128 v[16:19], v16 offset:3072
	ds_read_b128 v[20:23], v32
	ds_read_b128 v[24:27], v32 offset:1024
	ds_read_b128 v[28:31], v32 offset:2048
	ds_read_b128 v[32:35], v32 offset:3072
	s_mov_b32 m0, s29
	v_lshl_add_u64 v[214:215], s[64:65], 0, v[214:215]
	ds_read_b128 v[36:39], v245 offset:32768
	ds_read_b128 v[40:43], v245 offset:33792
	ds_read_b128 v[44:47], v245 offset:34816
	ds_read_b128 v[48:51], v245 offset:35840
	ds_read_b128 v[52:55], v245 offset:36864
	ds_read_b128 v[56:59], v245 offset:37888
	ds_read_b128 v[60:63], v245 offset:38912
	ds_read_b128 v[64:67], v245 offset:39936
	global_load_lds_dwordx4 v[214:215], off
	v_lshl_add_u64 v[212:213], s[64:65], 0, v[212:213]
	s_mov_b32 m0, s66
	s_nop 0
	global_load_lds_dwordx4 v[212:213], off
	s_waitcnt vmcnt(8)
	s_waitcnt lgkmcnt(0)
	s_barrier
	s_setprio 1
	s_waitcnt lgkmcnt(0)
	v_mfma_scale_f32_16x16x128_f8f6f4 v[192:195], v[4:11], v[36:43], v[192:195], v219, v216 op_sel_hi:[0,0,0]
	v_mfma_scale_f32_16x16x128_f8f6f4 v[188:191], v[12:19], v[36:43], v[188:191], v219, v216 op_sel_hi:[0,0,0]
	v_mfma_scale_f32_16x16x128_f8f6f4 v[176:179], v[4:11], v[44:51], v[176:179], v219, v216 op_sel_hi:[0,0,0]
	v_mfma_scale_f32_16x16x128_f8f6f4 v[172:175], v[12:19], v[44:51], v[172:175], v219, v216 op_sel_hi:[0,0,0]
	v_mfma_scale_f32_16x16x128_f8f6f4 v[160:163], v[4:11], v[52:59], v[160:163], v219, v216 op_sel_hi:[0,0,0]
	v_mfma_scale_f32_16x16x128_f8f6f4 v[156:159], v[12:19], v[52:59], v[156:159], v219, v216 op_sel_hi:[0,0,0]
	v_mfma_scale_f32_16x16x128_f8f6f4 v[144:147], v[4:11], v[60:67], v[144:147], v219, v216 op_sel_hi:[0,0,0]
	v_mfma_scale_f32_16x16x128_f8f6f4 v[140:143], v[12:19], v[60:67], v[140:143], v219, v216 op_sel_hi:[0,0,0]
	s_setprio 0
	s_setprio 1
	v_mfma_scale_f32_16x16x128_f8f6f4 v[184:187], v[20:27], v[36:43], v[184:187], v219, v216 op_sel_hi:[0,0,0]
	v_mfma_scale_f32_16x16x128_f8f6f4 v[180:183], v[28:35], v[36:43], v[180:183], v219, v216 op_sel_hi:[0,0,0]
	v_mfma_scale_f32_16x16x128_f8f6f4 v[168:171], v[20:27], v[44:51], v[168:171], v219, v216 op_sel_hi:[0,0,0]
	v_mfma_scale_f32_16x16x128_f8f6f4 v[164:167], v[28:35], v[44:51], v[164:167], v219, v216 op_sel_hi:[0,0,0]
	v_mfma_scale_f32_16x16x128_f8f6f4 v[152:155], v[20:27], v[52:59], v[152:155], v219, v216 op_sel_hi:[0,0,0]
	v_mfma_scale_f32_16x16x128_f8f6f4 v[148:151], v[28:35], v[52:59], v[148:151], v219, v216 op_sel_hi:[0,0,0]
	v_mfma_scale_f32_16x16x128_f8f6f4 v[136:139], v[20:27], v[60:67], v[136:139], v219, v216 op_sel_hi:[0,0,0]
	v_mfma_scale_f32_16x16x128_f8f6f4 v[132:135], v[28:35], v[60:67], v[132:135], v219, v216 op_sel_hi:[0,0,0]
	s_setprio 0
	s_barrier
	s_add_i32 s64, s82, s8
	v_lshl_add_u64 v[212:213], s[62:63], 0, v[198:199]
	s_mov_b32 m0, s64
	ds_read_b128 v[36:39], v245 offset:49152
	ds_read_b128 v[40:43], v245 offset:50176
	ds_read_b128 v[44:47], v245 offset:51200
	ds_read_b128 v[48:51], v245 offset:52224
	ds_read_b128 v[52:55], v245 offset:53248
	ds_read_b128 v[56:59], v245 offset:54272
	ds_read_b128 v[60:63], v245 offset:55296
	ds_read_b128 v[64:67], v245 offset:56320
	global_load_lds_dwordx4 v[212:213], off
	s_add_i32 m0, s64, 0x2000
	s_add_u32 s60, s60, 0x8080
	v_lshl_add_u64 v[212:213], s[62:63], 0, v[196:197]
	s_addc_u32 s61, s61, 0
	s_add_i32 s62, s83, s8
	global_load_lds_dwordx4 v[212:213], off
	v_lshl_add_u64 v[212:213], s[60:61], 0, v[198:199]
	s_mov_b32 m0, s62
	s_nop 0
	global_load_lds_dwordx4 v[212:213], off
	v_lshl_add_u64 v[212:213], s[60:61], 0, v[196:197]
	s_add_i32 m0, s62, 0x2000
	s_nop 0
	global_load_lds_dwordx4 v[212:213], off
	s_mov_b32 m0, s67
	s_nop 0
	global_load_lds_dwordx4 v200, s[56:57]
	s_mov_b32 m0, s68
	s_nop 0
	global_load_lds_dwordx4 v202, s[56:57]
	s_waitcnt vmcnt(8)
	s_waitcnt lgkmcnt(0)
	s_barrier
	s_setprio 1
	s_waitcnt lgkmcnt(0)
	v_mfma_scale_f32_16x16x128_f8f6f4 v[128:131], v[4:11], v[36:43], v[128:131], v219, v216 op_sel_hi:[0,0,0]
	v_mfma_scale_f32_16x16x128_f8f6f4 v[124:127], v[12:19], v[36:43], v[124:127], v219, v216 op_sel_hi:[0,0,0]
	v_mfma_scale_f32_16x16x128_f8f6f4 v[112:115], v[4:11], v[44:51], v[112:115], v219, v216 op_sel_hi:[0,0,0]
	v_mfma_scale_f32_16x16x128_f8f6f4 v[108:111], v[12:19], v[44:51], v[108:111], v219, v216 op_sel_hi:[0,0,0]
	v_mfma_scale_f32_16x16x128_f8f6f4 v[96:99], v[4:11], v[52:59], v[96:99], v219, v216 op_sel_hi:[0,0,0]
	v_mfma_scale_f32_16x16x128_f8f6f4 v[92:95], v[12:19], v[52:59], v[92:95], v219, v216 op_sel_hi:[0,0,0]
	v_mfma_scale_f32_16x16x128_f8f6f4 v[80:83], v[4:11], v[60:67], v[80:83], v219, v216 op_sel_hi:[0,0,0]
	v_mfma_scale_f32_16x16x128_f8f6f4 v[76:79], v[12:19], v[60:67], v[76:79], v219, v216 op_sel_hi:[0,0,0]
	s_setprio 0
	s_setprio 1
	v_mfma_scale_f32_16x16x128_f8f6f4 v[120:123], v[20:27], v[36:43], v[120:123], v219, v216 op_sel_hi:[0,0,0]
	v_mfma_scale_f32_16x16x128_f8f6f4 v[116:119], v[28:35], v[36:43], v[116:119], v219, v216 op_sel_hi:[0,0,0]
	v_mfma_scale_f32_16x16x128_f8f6f4 v[104:107], v[20:27], v[44:51], v[104:107], v219, v216 op_sel_hi:[0,0,0]
	v_mfma_scale_f32_16x16x128_f8f6f4 v[100:103], v[28:35], v[44:51], v[100:103], v219, v216 op_sel_hi:[0,0,0]
	v_mfma_scale_f32_16x16x128_f8f6f4 v[88:91], v[20:27], v[52:59], v[88:91], v219, v216 op_sel_hi:[0,0,0]
	v_mfma_scale_f32_16x16x128_f8f6f4 v[84:87], v[28:35], v[52:59], v[84:87], v219, v216 op_sel_hi:[0,0,0]
	v_mfma_scale_f32_16x16x128_f8f6f4 v[72:75], v[20:27], v[60:67], v[72:75], v219, v216 op_sel_hi:[0,0,0]
	v_mfma_scale_f32_16x16x128_f8f6f4 v[68:71], v[28:35], v[60:67], v[68:71], v219, v216 op_sel_hi:[0,0,0]
	s_setprio 0
	s_barrier
	s_add_u32 s2, s2, 0x100
	s_addc_u32 s3, s3, 0
	s_cmp_ge_i32 s79, s5
	s_cbranch_scc1 .LBB0_668
; #define PG8_STAGEA(bufoff, gbase, h) do { if constexpr (GATHER) { PG8_STAGE(bufoff, gbase, vA[h]); } else { PG8_STAGE(bufoff, (gbase) + (h) * hstepA, voffA); } } while (0)
; #define PG8_LDA(dst, b, h) do { _Pragma("unroll") for (int m = 0; m < 4; ++m) _Pragma("unroll") for (int k = 0; k < 2; ++k) dst[m][k] = *(const LAS bf16x8*)(lds + PG8_SA(b, h) + aoff + m * 2048 + k * 1024); } while (0)
; #define PG8_SCHED __builtin_amdgcn_sched_barrier(0)
; template <class Epi, class Sched>
; __device__ __forceinline__ void gemm_phase(const int tid, LAS unsigned char* lds, const char* Abase, const int lda, const int ldb, const int K, const Sched& S, const Epi& E) {
;     ...
;         for (int t = 0; t < nt; t += 2) {
;             const bool last = (t == nt - 2);
;             const char* a1 = cA + (size_t)(t + 1) * kstepA;
;             const char* a2 = last ? nA : cA + (size_t)(t + 2) * kstepA; const char* b2 = last ? nB : cB + (size_t)(t + 2) * kstep;
;             const char* a3 = a2 + kstepA; const char* b3 = b2 + kstep;
;             PG8_LDB(B0, 0, 0); PG8_LDB(B1, 0, 1); PG8_SCHED; PG8_LDA(At, 0, 0); PG8_STAGEA(PG8_SA(1, 1), a1, 1);
.LBB0_665:
	v_add_u32_e32 v4, 0, v201
	v_add_u32_e32 v5, 0x10000, v4
	v_add_u32_e32 v16, 0x14000, v4
	ds_read_b128 v[20:23], v5
	ds_read_b128 v[24:27], v5 offset:1024
	ds_read_b128 v[28:31], v5 offset:2048
	ds_read_b128 v[32:35], v5 offset:3072
	ds_read_b128 v[4:7], v16
	ds_read_b128 v[8:11], v16 offset:1024
	ds_read_b128 v[12:15], v16 offset:2048
	ds_read_b128 v[16:19], v16 offset:3072
	s_cmp_eq_u32 s70, s79
	s_cselect_b64 s[60:61], -1, 0
	s_add_u32 s56, s38, s2
	s_addc_u32 s57, s39, s3
	s_add_u32 s56, s56, 0xffffff80
	s_addc_u32 s57, s57, -1
	s_add_i32 m0, s9, 0xc000
	s_add_i32 s62, s9, 0xe000
	s_cmp_lg_u32 s70, s79
	ds_read_b128 v[60:63], v245
	ds_read_b128 v[64:67], v245 offset:1024
	ds_read_b128 v[52:55], v245 offset:2048
	ds_read_b128 v[56:59], v245 offset:3072
	ds_read_b128 v[44:47], v245 offset:4096
	ds_read_b128 v[48:51], v245 offset:5120
	ds_read_b128 v[36:39], v245 offset:6144
	ds_read_b128 v[40:43], v245 offset:7168
	global_load_lds_dwordx4 v2, s[56:57]
	s_mov_b32 m0, s62
	s_nop 0
	global_load_lds_dwordx4 v204, s[56:57]
	s_cbranch_scc0 .LBB0_663
	v_mov_b32_e32 v205, v3
	v_mov_b64_e32 v[212:213], v[204:205]
	v_mov_b64_e32 v[214:215], v[2:3]
	s_cmp_eq_u32 s79, 0
	s_cbranch_scc1 .Lpeel_ao
	s_branch .LBB0_664

; #define PG8_STAGEA(bufoff, gbase, h) do { if constexpr (GATHER) { PG8_STAGE(bufoff, gbase, vA[h]); } else { PG8_STAGE(bufoff, (gbase) + (h) * hstepA, voffA); } } while (0)
; #define PG8_LDA(dst, b, h) do { _Pragma("unroll") for (int m = 0; m < 4; ++m) _Pragma("unroll") for (int k = 0; k < 2; ++k) dst[m][k] = *(const LAS bf16x8*)(lds + PG8_SA(b, h) + aoff + m * 2048 + k * 1024); } while (0)
; #define PG8_MM(ai, bj, At, Bt) do { if constexpr (Epi::F8MMA) PG8_MMA8(ai, bj, At, Bt##8); else PG8_MMA(ai, bj, At, Bt); } while (0)
; #define PG8_WAIT_V(n) asm volatile("s_waitcnt vmcnt(" #n ")" ::: "memory")
; #define PG8_WAIT_L(n) asm volatile("s_waitcnt lgkmcnt(" #n ")" ::: "memory")
; #define PG8_BAR __builtin_amdgcn_s_barrier()
; #define PG8_SCHED __builtin_amdgcn_sched_barrier(0)
; template <class Epi, class Sched>
; __device__ __forceinline__ void gemm_phase(const int tid, LAS unsigned char* lds, const char* Abase, const int lda, const int ldb, const int K, const Sched& S, const Epi& E) {
;     ...
;             PG8_LDB(B0, 0, 0); PG8_LDB(B1, 0, 1); PG8_SCHED; PG8_LDA(At, 0, 0); PG8_STAGEA(PG8_SA(1, 1), a1, 1);
;             if constexpr (GATHER) { if (last) {
; #pragma unroll
;                 for (int h = 0; h < 2; ++h)
; #pragma unroll
;                     for (int i = 0; i < 2; ++i) vA[h][i] = vAn[h][i]; } }
;             PG8_WAIT_V(8); PG8_WAIT_L(0); PG8_BAR; PG8_MM(0, 0, At, B0); PG8_MM(0, 1, At, B1); PG8_BAR; PG8_SCHED;
;             PG8_LDA(At, 0, 1); PG8_STAGE(PG8_SB(0, 0), b2, voffB); PG8_STAGE(PG8_SB(0, 1), b2 + hstepB, voffB); PG8_STAGEA(PG8_SA(0, 0), a2, 0);
;             PG8_WAIT_V(8); PG8_WAIT_L(0); PG8_BAR; PG8_MM(1, 0, At, B0); PG8_MM(1, 1, At, B1); PG8_BAR; PG8_SCHED;
.LBB0_768:
	s_andn2_b64 vcc, exec, s[48:49]
	s_cbranch_vccnz .LBB0_774
	v_mov_b32_e32 v209, v3
	v_mov_b32_e32 v211, v3
	s_mov_b32 s83, 0
	s_mov_b64 s[2:3], 0x100
	s_waitcnt lgkmcnt(0)
	s_branch .LBB0_772
.Lpeel_pi:
	s_add_i32 s83, s83, 2
	s_and_b64 s[60:61], s[62:63], exec
	s_cselect_b32 s61, 0, s2
	s_cselect_b32 s60, 0, s3
	s_add_u32 s66, s42, s61
	s_addc_u32 s67, s43, s60
	s_add_u32 s64, s56, s2
	s_addc_u32 s65, s57, s3
	s_add_u32 s60, s66, 0x80
	s_addc_u32 s61, s67, 0
	s_waitcnt vmcnt(8)
	s_and_b64 s[62:63], s[62:63], exec
	s_waitcnt lgkmcnt(0)
	s_cselect_b32 s62, s54, s64
	s_cselect_b32 s63, s55, s65
	s_add_u32 s64, s62, 0x80
	s_addc_u32 s65, s63, 0
	s_barrier
	s_setprio 1
	s_waitcnt lgkmcnt(0)
	v_mfma_scale_f32_16x16x128_f8f6f4 v[192:195], v[20:27], v[60:67], 0, v220, v216 op_sel_hi:[0,0,0]
	v_mfma_scale_f32_16x16x128_f8f6f4 v[188:191], v[28:35], v[60:67], 0, v220, v216 op_sel_hi:[0,0,0]
	v_mfma_scale_f32_16x16x128_f8f6f4 v[176:179], v[20:27], v[52:59], 0, v220, v216 op_sel_hi:[0,0,0]
	v_mfma_scale_f32_16x16x128_f8f6f4 v[172:175], v[28:35], v[52:59], 0, v220, v216 op_sel_hi:[0,0,0]
	v_mfma_scale_f32_16x16x128_f8f6f4 v[160:163], v[20:27], v[44:51], 0, v220, v216 op_sel_hi:[0,0,0]
	v_mfma_scale_f32_16x16x128_f8f6f4 v[156:159], v[28:35], v[44:51], 0, v220, v216 op_sel_hi:[0,0,0]
	v_mfma_scale_f32_16x16x128_f8f6f4 v[144:147], v[20:27], v[36:43], 0, v220, v216 op_sel_hi:[0,0,0]
	v_mfma_scale_f32_16x16x128_f8f6f4 v[140:143], v[28:35], v[36:43], 0, v220, v216 op_sel_hi:[0,0,0]
	s_setprio 0
	s_setprio 1
	v_mfma_scale_f32_16x16x128_f8f6f4 v[184:187], v[4:11], v[60:67], 0, v220, v216 op_sel_hi:[0,0,0]
	v_mfma_scale_f32_16x16x128_f8f6f4 v[180:183], v[12:19], v[60:67], 0, v220, v216 op_sel_hi:[0,0,0]
	v_mfma_scale_f32_16x16x128_f8f6f4 v[168:171], v[4:11], v[52:59], 0, v220, v216 op_sel_hi:[0,0,0]
	v_mfma_scale_f32_16x16x128_f8f6f4 v[164:167], v[12:19], v[52:59], 0, v220, v216 op_sel_hi:[0,0,0]
	v_mfma_scale_f32_16x16x128_f8f6f4 v[152:155], v[4:11], v[44:51], 0, v220, v216 op_sel_hi:[0,0,0]
	v_mfma_scale_f32_16x16x128_f8f6f4 v[148:151], v[12:19], v[44:51], 0, v220, v216 op_sel_hi:[0,0,0]
	v_mfma_scale_f32_16x16x128_f8f6f4 v[136:139], v[4:11], v[36:43], 0, v220, v216 op_sel_hi:[0,0,0]
	v_mfma_scale_f32_16x16x128_f8f6f4 v[132:135], v[12:19], v[36:43], 0, v220, v216 op_sel_hi:[0,0,0]
	s_setprio 0
	s_barrier
	s_mov_b32 m0, s10
	v_lshl_add_u64 v[228:229], s[62:63], 0, v[198:199]
	s_add_u32 s86, s62, 0x8000
	ds_read_b128 v[36:39], v243 offset:16384
	ds_read_b128 v[40:43], v243 offset:17408
	ds_read_b128 v[44:47], v243 offset:18432
	ds_read_b128 v[48:51], v243 offset:19456
	ds_read_b128 v[52:55], v243 offset:20480
	ds_read_b128 v[56:59], v243 offset:21504
	ds_read_b128 v[60:63], v243 offset:22528
	ds_read_b128 v[64:67], v243 offset:23552
	global_load_lds_dwordx4 v[228:229], off
	v_lshl_add_u64 v[228:229], s[62:63], 0, v[196:197]
	s_mov_b32 m0, s11
	s_addc_u32 s87, s63, 0
	global_load_lds_dwordx4 v[228:229], off
	v_lshl_add_u64 v[228:229], s[86:87], 0, v[198:199]
	s_mov_b32 m0, s22
	s_nop 0
	global_load_lds_dwordx4 v[228:229], off
	v_lshl_add_u64 v[228:229], s[86:87], 0, v[196:197]
	s_mov_b32 m0, s25
	s_nop 0
	global_load_lds_dwordx4 v[228:229], off
	s_mov_b32 m0, s9
	s_nop 0
	global_load_lds_dwordx4 v200, s[66:67]
	s_mov_b32 m0, s28
	s_nop 0
	global_load_lds_dwordx4 v202, s[66:67]
	s_waitcnt vmcnt(8)
	s_waitcnt lgkmcnt(0)
	s_barrier
	s_setprio 1
	s_waitcnt lgkmcnt(0)
	v_mfma_scale_f32_16x16x128_f8f6f4 v[128:131], v[20:27], v[36:43], 0, v220, v216 op_sel_hi:[0,0,0]
	v_mfma_scale_f32_16x16x128_f8f6f4 v[124:127], v[28:35], v[36:43], 0, v220, v216 op_sel_hi:[0,0,0]
	v_mfma_scale_f32_16x16x128_f8f6f4 v[112:115], v[20:27], v[44:51], 0, v220, v216 op_sel_hi:[0,0,0]
	v_mfma_scale_f32_16x16x128_f8f6f4 v[108:111], v[28:35], v[44:51], 0, v220, v216 op_sel_hi:[0,0,0]
	v_mfma_scale_f32_16x16x128_f8f6f4 v[96:99], v[20:27], v[52:59], 0, v220, v216 op_sel_hi:[0,0,0]
	v_mfma_scale_f32_16x16x128_f8f6f4 v[92:95], v[28:35], v[52:59], 0, v220, v216 op_sel_hi:[0,0,0]
	v_mfma_scale_f32_16x16x128_f8f6f4 v[80:83], v[20:27], v[60:67], 0, v220, v216 op_sel_hi:[0,0,0]
	v_mfma_scale_f32_16x16x128_f8f6f4 v[76:79], v[28:35], v[60:67], 0, v220, v216 op_sel_hi:[0,0,0]
	s_setprio 0
	s_setprio 1
	v_mfma_scale_f32_16x16x128_f8f6f4 v[120:123], v[4:11], v[36:43], 0, v220, v216 op_sel_hi:[0,0,0]
	v_mfma_scale_f32_16x16x128_f8f6f4 v[116:119], v[12:19], v[36:43], 0, v220, v216 op_sel_hi:[0,0,0]
	v_mfma_scale_f32_16x16x128_f8f6f4 v[104:107], v[4:11], v[44:51], 0, v220, v216 op_sel_hi:[0,0,0]
	v_mfma_scale_f32_16x16x128_f8f6f4 v[100:103], v[12:19], v[44:51], 0, v220, v216 op_sel_hi:[0,0,0]
	v_mfma_scale_f32_16x16x128_f8f6f4 v[88:91], v[4:11], v[52:59], 0, v220, v216 op_sel_hi:[0,0,0]
	v_mfma_scale_f32_16x16x128_f8f6f4 v[84:87], v[12:19], v[52:59], 0, v220, v216 op_sel_hi:[0,0,0]
	v_mfma_scale_f32_16x16x128_f8f6f4 v[72:75], v[4:11], v[60:67], 0, v220, v216 op_sel_hi:[0,0,0]
	v_mfma_scale_f32_16x16x128_f8f6f4 v[68:71], v[12:19], v[60:67], 0, v220, v216 op_sel_hi:[0,0,0]
	s_setprio 0
	s_barrier
	s_branch .Lmid_pi

; #define PG8_STAGEA(bufoff, gbase, h) do { if constexpr (GATHER) { PG8_STAGE(bufoff, gbase, vA[h]); } else { PG8_STAGE(bufoff, (gbase) + (h) * hstepA, voffA); } } while (0)
; #define PG8_LDA(dst, b, h) do { _Pragma("unroll") for (int m = 0; m < 4; ++m) _Pragma("unroll") for (int k = 0; k < 2; ++k) dst[m][k] = *(const LAS bf16x8*)(lds + PG8_SA(b, h) + aoff + m * 2048 + k * 1024); } while (0)
; #define PG8_MM(ai, bj, At, Bt) do { if constexpr (Epi::F8MMA) PG8_MMA8(ai, bj, At, Bt##8); else PG8_MMA(ai, bj, At, Bt); } while (0)
; #define PG8_WAIT_V(n) asm volatile("s_waitcnt vmcnt(" #n ")" ::: "memory")
; #define PG8_WAIT_L(n) asm volatile("s_waitcnt lgkmcnt(" #n ")" ::: "memory")
; #define PG8_BAR __builtin_amdgcn_s_barrier()
; #define PG8_SCHED __builtin_amdgcn_sched_barrier(0)
; template <class Epi, class Sched>
; __device__ __forceinline__ void gemm_phase(const int tid, LAS unsigned char* lds, const char* Abase, const int lda, const int ldb, const int K, const Sched& S, const Epi& E) {
;     ...
;             PG8_LDB(B0, 1, 0); PG8_LDB(B1, 1, 1); PG8_SCHED; PG8_LDA(At, 1, 0); PG8_STAGEA(PG8_SA(0, 1), a2, 1);
;             PG8_WAIT_V(8); PG8_WAIT_L(0); PG8_BAR; PG8_MM(0, 0, At, B0); PG8_MM(0, 1, At, B1); PG8_BAR; PG8_SCHED;
;             PG8_LDA(At, 1, 1); PG8_STAGE(PG8_SB(1, 0), b3, voffB); PG8_STAGE(PG8_SB(1, 1), b3 + hstepB, voffB); PG8_STAGEA(PG8_SA(1, 0), a3, 0);
;             PG8_WAIT_V(8); PG8_WAIT_L(0); PG8_BAR; PG8_MM(1, 0, At, B0); PG8_MM(1, 1, At, B1); PG8_BAR; PG8_SCHED;
;         }
.Lmid_pi:
	s_add_i32 s86, 0, 0x18000
	s_add_i32 s87, 0, 0x1c000
	v_add_u32_e32 v16, s86, v201
	v_add_u32_e32 v32, s87, v201
	ds_read_b128 v[4:7], v16
	ds_read_b128 v[8:11], v16 offset:1024
	ds_read_b128 v[12:15], v16 offset:2048
	ds_read_b128 v[16:19], v16 offset:3072
	ds_read_b128 v[20:23], v32
	ds_read_b128 v[24:27], v32 offset:1024
	ds_read_b128 v[28:31], v32 offset:2048
	ds_read_b128 v[32:35], v32 offset:3072
	s_mov_b32 m0, s29
	v_lshl_add_u64 v[214:215], s[66:67], 0, v[214:215]
	ds_read_b128 v[36:39], v243 offset:32768
	ds_read_b128 v[40:43], v243 offset:33792
	ds_read_b128 v[44:47], v243 offset:34816
	ds_read_b128 v[48:51], v243 offset:35840
	ds_read_b128 v[52:55], v243 offset:36864
	ds_read_b128 v[56:59], v243 offset:37888
	ds_read_b128 v[60:63], v243 offset:38912
	ds_read_b128 v[64:67], v243 offset:39936
	global_load_lds_dwordx4 v[214:215], off
	v_lshl_add_u64 v[212:213], s[66:67], 0, v[212:213]
	s_mov_b32 m0, s68
	s_nop 0
	global_load_lds_dwordx4 v[212:213], off
	s_waitcnt vmcnt(8)
	s_waitcnt lgkmcnt(0)
	s_barrier
	s_setprio 1
	s_waitcnt lgkmcnt(0)
	v_mfma_scale_f32_16x16x128_f8f6f4 v[192:195], v[4:11], v[36:43], v[192:195], v220, v216 op_sel_hi:[0,0,0]
	v_mfma_scale_f32_16x16x128_f8f6f4 v[188:191], v[12:19], v[36:43], v[188:191], v220, v216 op_sel_hi:[0,0,0]
	v_mfma_scale_f32_16x16x128_f8f6f4 v[176:179], v[4:11], v[44:51], v[176:179], v220, v216 op_sel_hi:[0,0,0]
	v_mfma_scale_f32_16x16x128_f8f6f4 v[172:175], v[12:19], v[44:51], v[172:175], v220, v216 op_sel_hi:[0,0,0]
	v_mfma_scale_f32_16x16x128_f8f6f4 v[160:163], v[4:11], v[52:59], v[160:163], v220, v216 op_sel_hi:[0,0,0]
	v_mfma_scale_f32_16x16x128_f8f6f4 v[156:159], v[12:19], v[52:59], v[156:159], v220, v216 op_sel_hi:[0,0,0]
	v_mfma_scale_f32_16x16x128_f8f6f4 v[144:147], v[4:11], v[60:67], v[144:147], v220, v216 op_sel_hi:[0,0,0]
	v_mfma_scale_f32_16x16x128_f8f6f4 v[140:143], v[12:19], v[60:67], v[140:143], v220, v216 op_sel_hi:[0,0,0]
	s_setprio 0
	s_setprio 1
	v_mfma_scale_f32_16x16x128_f8f6f4 v[184:187], v[20:27], v[36:43], v[184:187], v220, v216 op_sel_hi:[0,0,0]
	v_mfma_scale_f32_16x16x128_f8f6f4 v[180:183], v[28:35], v[36:43], v[180:183], v220, v216 op_sel_hi:[0,0,0]
	v_mfma_scale_f32_16x16x128_f8f6f4 v[168:171], v[20:27], v[44:51], v[168:171], v220, v216 op_sel_hi:[0,0,0]
	v_mfma_scale_f32_16x16x128_f8f6f4 v[164:167], v[28:35], v[44:51], v[164:167], v220, v216 op_sel_hi:[0,0,0]
	v_mfma_scale_f32_16x16x128_f8f6f4 v[152:155], v[20:27], v[52:59], v[152:155], v220, v216 op_sel_hi:[0,0,0]
	v_mfma_scale_f32_16x16x128_f8f6f4 v[148:151], v[28:35], v[52:59], v[148:151], v220, v216 op_sel_hi:[0,0,0]
	v_mfma_scale_f32_16x16x128_f8f6f4 v[136:139], v[20:27], v[60:67], v[136:139], v220, v216 op_sel_hi:[0,0,0]
	v_mfma_scale_f32_16x16x128_f8f6f4 v[132:135], v[28:35], v[60:67], v[132:135], v220, v216 op_sel_hi:[0,0,0]
	s_setprio 0
	s_barrier
	s_add_i32 s66, s86, s8
	v_lshl_add_u64 v[212:213], s[64:65], 0, v[198:199]
	s_mov_b32 m0, s66
	ds_read_b128 v[36:39], v243 offset:49152
	ds_read_b128 v[40:43], v243 offset:50176
	ds_read_b128 v[44:47], v243 offset:51200
	ds_read_b128 v[48:51], v243 offset:52224
	ds_read_b128 v[52:55], v243 offset:53248
	ds_read_b128 v[56:59], v243 offset:54272
	ds_read_b128 v[60:63], v243 offset:55296
	ds_read_b128 v[64:67], v243 offset:56320
	global_load_lds_dwordx4 v[212:213], off
	s_add_i32 m0, s66, 0x2000
	s_add_u32 s62, s62, 0x8080
	v_lshl_add_u64 v[212:213], s[64:65], 0, v[196:197]
	s_addc_u32 s63, s63, 0
	s_add_i32 s64, s87, s8
	global_load_lds_dwordx4 v[212:213], off
	v_lshl_add_u64 v[212:213], s[62:63], 0, v[198:199]
	s_mov_b32 m0, s64
	s_nop 0
	global_load_lds_dwordx4 v[212:213], off
	v_lshl_add_u64 v[212:213], s[62:63], 0, v[196:197]
	s_add_i32 m0, s64, 0x2000
	s_nop 0
	global_load_lds_dwordx4 v[212:213], off
	s_mov_b32 m0, s69
	s_nop 0
	global_load_lds_dwordx4 v200, s[60:61]
	s_mov_b32 m0, s70
	s_nop 0
	global_load_lds_dwordx4 v202, s[60:61]
	s_waitcnt vmcnt(8)
	s_waitcnt lgkmcnt(0)
	s_barrier
	s_setprio 1
	s_waitcnt lgkmcnt(0)
	v_mfma_scale_f32_16x16x128_f8f6f4 v[128:131], v[4:11], v[36:43], v[128:131], v220, v216 op_sel_hi:[0,0,0]
	v_mfma_scale_f32_16x16x128_f8f6f4 v[124:127], v[12:19], v[36:43], v[124:127], v220, v216 op_sel_hi:[0,0,0]
	v_mfma_scale_f32_16x16x128_f8f6f4 v[112:115], v[4:11], v[44:51], v[112:115], v220, v216 op_sel_hi:[0,0,0]
	v_mfma_scale_f32_16x16x128_f8f6f4 v[108:111], v[12:19], v[44:51], v[108:111], v220, v216 op_sel_hi:[0,0,0]
	v_mfma_scale_f32_16x16x128_f8f6f4 v[96:99], v[4:11], v[52:59], v[96:99], v220, v216 op_sel_hi:[0,0,0]
	v_mfma_scale_f32_16x16x128_f8f6f4 v[92:95], v[12:19], v[52:59], v[92:95], v220, v216 op_sel_hi:[0,0,0]
	v_mfma_scale_f32_16x16x128_f8f6f4 v[80:83], v[4:11], v[60:67], v[80:83], v220, v216 op_sel_hi:[0,0,0]
	v_mfma_scale_f32_16x16x128_f8f6f4 v[76:79], v[12:19], v[60:67], v[76:79], v220, v216 op_sel_hi:[0,0,0]
	s_setprio 0
	s_setprio 1
	v_mfma_scale_f32_16x16x128_f8f6f4 v[120:123], v[20:27], v[36:43], v[120:123], v220, v216 op_sel_hi:[0,0,0]
	v_mfma_scale_f32_16x16x128_f8f6f4 v[116:119], v[28:35], v[36:43], v[116:119], v220, v216 op_sel_hi:[0,0,0]
	v_mfma_scale_f32_16x16x128_f8f6f4 v[104:107], v[20:27], v[44:51], v[104:107], v220, v216 op_sel_hi:[0,0,0]
	v_mfma_scale_f32_16x16x128_f8f6f4 v[100:103], v[28:35], v[44:51], v[100:103], v220, v216 op_sel_hi:[0,0,0]
	v_mfma_scale_f32_16x16x128_f8f6f4 v[88:91], v[20:27], v[52:59], v[88:91], v220, v216 op_sel_hi:[0,0,0]
	v_mfma_scale_f32_16x16x128_f8f6f4 v[84:87], v[28:35], v[52:59], v[84:87], v220, v216 op_sel_hi:[0,0,0]
	v_mfma_scale_f32_16x16x128_f8f6f4 v[72:75], v[20:27], v[60:67], v[72:75], v220, v216 op_sel_hi:[0,0,0]
	v_mfma_scale_f32_16x16x128_f8f6f4 v[68:71], v[28:35], v[60:67], v[68:71], v220, v216 op_sel_hi:[0,0,0]
	s_setprio 0
	s_barrier
	s_add_u32 s2, s2, 0x100
	s_addc_u32 s3, s3, 0
	s_cmp_ge_i32 s83, s5
	s_cbranch_scc1 .LBB0_775
; #define PG8_STAGEA(bufoff, gbase, h) do { if constexpr (GATHER) { PG8_STAGE(bufoff, gbase, vA[h]); } else { PG8_STAGE(bufoff, (gbase) + (h) * hstepA, voffA); } } while (0)
; #define PG8_LDA(dst, b, h) do { _Pragma("unroll") for (int m = 0; m < 4; ++m) _Pragma("unroll") for (int k = 0; k < 2; ++k) dst[m][k] = *(const LAS bf16x8*)(lds + PG8_SA(b, h) + aoff + m * 2048 + k * 1024); } while (0)
; #define PG8_SCHED __builtin_amdgcn_sched_barrier(0)
; template <class Epi, class Sched>
; __device__ __forceinline__ void gemm_phase(const int tid, LAS unsigned char* lds, const char* Abase, const int lda, const int ldb, const int K, const Sched& S, const Epi& E) {
;     ...
;         for (int t = 0; t < nt; t += 2) {
;             const bool last = (t == nt - 2);
;             const char* a1 = cA + (size_t)(t + 1) * kstepA;
;             const char* a2 = last ? nA : cA + (size_t)(t + 2) * kstepA; const char* b2 = last ? nB : cB + (size_t)(t + 2) * kstep;
;             const char* a3 = a2 + kstepA; const char* b3 = b2 + kstep;
;             PG8_LDB(B0, 0, 0); PG8_LDB(B1, 0, 1); PG8_SCHED; PG8_LDA(At, 0, 0); PG8_STAGEA(PG8_SA(1, 1), a1, 1);
.LBB0_772:
	v_add_u32_e32 v4, 0, v201
	v_add_u32_e32 v5, 0x10000, v4
	v_add_u32_e32 v16, 0x14000, v4
	ds_read_b128 v[20:23], v5
	ds_read_b128 v[24:27], v5 offset:1024
	ds_read_b128 v[28:31], v5 offset:2048
	ds_read_b128 v[32:35], v5 offset:3072
	ds_read_b128 v[4:7], v16
	ds_read_b128 v[8:11], v16 offset:1024
	ds_read_b128 v[12:15], v16 offset:2048
	ds_read_b128 v[16:19], v16 offset:3072
	s_cmp_eq_u32 s72, s83
	s_cselect_b64 s[62:63], -1, 0
	s_add_u32 s60, s42, s2
	s_addc_u32 s61, s43, s3
	s_add_u32 s60, s60, 0xffffff80
	s_addc_u32 s61, s61, -1
	s_add_i32 m0, s9, 0xc000
	s_add_i32 s64, s9, 0xe000
	s_cmp_lg_u32 s72, s83
	ds_read_b128 v[60:63], v243
	ds_read_b128 v[64:67], v243 offset:1024
	ds_read_b128 v[52:55], v243 offset:2048
	ds_read_b128 v[56:59], v243 offset:3072
	ds_read_b128 v[44:47], v243 offset:4096
	ds_read_b128 v[48:51], v243 offset:5120
	ds_read_b128 v[36:39], v243 offset:6144
	ds_read_b128 v[40:43], v243 offset:7168
	global_load_lds_dwordx4 v2, s[60:61]
	s_mov_b32 m0, s64
	s_nop 0
	global_load_lds_dwordx4 v204, s[60:61]
	s_cbranch_scc0 .LBB0_770
	v_mov_b32_e32 v205, v3
	v_mov_b64_e32 v[212:213], v[204:205]
	v_mov_b64_e32 v[214:215], v[2:3]
	s_cmp_eq_u32 s83, 0
	s_cbranch_scc1 .Lpeel_pi
	s_branch .LBB0_771

; #define PG8_STAGEA(bufoff, gbase, h) do { if constexpr (GATHER) { PG8_STAGE(bufoff, gbase, vA[h]); } else { PG8_STAGE(bufoff, (gbase) + (h) * hstepA, voffA); } } while (0)
; #define PG8_LDA(dst, b, h) do { _Pragma("unroll") for (int m = 0; m < 4; ++m) _Pragma("unroll") for (int k = 0; k < 2; ++k) dst[m][k] = *(const LAS bf16x8*)(lds + PG8_SA(b, h) + aoff + m * 2048 + k * 1024); } while (0)
; #define PG8_MM(ai, bj, At, Bt) do { if constexpr (Epi::F8MMA) PG8_MMA8(ai, bj, At, Bt##8); else PG8_MMA(ai, bj, At, Bt); } while (0)
; #define PG8_WAIT_V(n) asm volatile("s_waitcnt vmcnt(" #n ")" ::: "memory")
; #define PG8_WAIT_L(n) asm volatile("s_waitcnt lgkmcnt(" #n ")" ::: "memory")
; #define PG8_BAR __builtin_amdgcn_s_barrier()
; #define PG8_SCHED __builtin_amdgcn_sched_barrier(0)
; template <class Epi, class Sched>
; __device__ __forceinline__ void gemm_phase(const int tid, LAS unsigned char* lds, const char* Abase, const int lda, const int ldb, const int K, const Sched& S, const Epi& E) {
;     ...
;             PG8_LDB(B0, 0, 0); PG8_LDB(B1, 0, 1); PG8_SCHED; PG8_LDA(At, 0, 0); PG8_STAGEA(PG8_SA(1, 1), a1, 1);
;             if constexpr (GATHER) { if (last) {
; #pragma unroll
;                 for (int h = 0; h < 2; ++h)
; #pragma unroll
;                     for (int i = 0; i < 2; ++i) vA[h][i] = vAn[h][i]; } }
;             PG8_WAIT_V(8); PG8_WAIT_L(0); PG8_BAR; PG8_MM(0, 0, At, B0); PG8_MM(0, 1, At, B1); PG8_BAR; PG8_SCHED;
;             PG8_LDA(At, 0, 1); PG8_STAGE(PG8_SB(0, 0), b2, voffB); PG8_STAGE(PG8_SB(0, 1), b2 + hstepB, voffB); PG8_STAGEA(PG8_SA(0, 0), a2, 0);
;             PG8_WAIT_V(8); PG8_WAIT_L(0); PG8_BAR; PG8_MM(1, 0, At, B0); PG8_MM(1, 1, At, B1); PG8_BAR; PG8_SCHED;
.LBB0_1163:
	s_andn2_b64 vcc, exec, s[46:47]
	s_cbranch_vccnz .LBB0_1169
	v_mov_b32_e32 v207, v3
	v_mov_b32_e32 v209, v3
	s_mov_b32 s83, 0
	s_mov_b64 s[56:57], 0x100
	s_waitcnt lgkmcnt(0)
	s_branch .LBB0_1167
.Lpeel_po:
	s_add_i32 s83, s83, 2
	s_and_b64 s[60:61], s[62:63], exec
	s_cselect_b32 s61, 0, s56
	s_cselect_b32 s60, 0, s57
	s_add_u32 s66, s40, s61
	s_addc_u32 s67, s41, s60
	s_add_u32 s64, s54, s56
	s_addc_u32 s65, s55, s57
	s_add_u32 s60, s66, 0x80
	s_addc_u32 s61, s67, 0
	s_waitcnt vmcnt(8)
	s_and_b64 s[62:63], s[62:63], exec
	s_waitcnt lgkmcnt(0)
	s_cselect_b32 s62, s52, s64
	s_cselect_b32 s63, s53, s65
	s_add_u32 s64, s62, 0x80
	s_addc_u32 s65, s63, 0
	s_barrier
	s_setprio 1
	s_waitcnt lgkmcnt(0)
	v_mfma_scale_f32_16x16x128_f8f6f4 v[192:195], v[20:27], v[60:67], 0, v221, v216 op_sel_hi:[0,0,0]
	v_mfma_scale_f32_16x16x128_f8f6f4 v[188:191], v[28:35], v[60:67], 0, v221, v216 op_sel_hi:[0,0,0]
	v_mfma_scale_f32_16x16x128_f8f6f4 v[176:179], v[20:27], v[52:59], 0, v221, v216 op_sel_hi:[0,0,0]
	v_mfma_scale_f32_16x16x128_f8f6f4 v[172:175], v[28:35], v[52:59], 0, v221, v216 op_sel_hi:[0,0,0]
	v_mfma_scale_f32_16x16x128_f8f6f4 v[160:163], v[20:27], v[44:51], 0, v221, v216 op_sel_hi:[0,0,0]
	v_mfma_scale_f32_16x16x128_f8f6f4 v[156:159], v[28:35], v[44:51], 0, v221, v216 op_sel_hi:[0,0,0]
	v_mfma_scale_f32_16x16x128_f8f6f4 v[144:147], v[20:27], v[36:43], 0, v221, v216 op_sel_hi:[0,0,0]
	v_mfma_scale_f32_16x16x128_f8f6f4 v[140:143], v[28:35], v[36:43], 0, v221, v216 op_sel_hi:[0,0,0]
	s_setprio 0
	s_setprio 1
	v_mfma_scale_f32_16x16x128_f8f6f4 v[184:187], v[4:11], v[60:67], 0, v221, v216 op_sel_hi:[0,0,0]
	v_mfma_scale_f32_16x16x128_f8f6f4 v[180:183], v[12:19], v[60:67], 0, v221, v216 op_sel_hi:[0,0,0]
	v_mfma_scale_f32_16x16x128_f8f6f4 v[168:171], v[4:11], v[52:59], 0, v221, v216 op_sel_hi:[0,0,0]
	v_mfma_scale_f32_16x16x128_f8f6f4 v[164:167], v[12:19], v[52:59], 0, v221, v216 op_sel_hi:[0,0,0]
	v_mfma_scale_f32_16x16x128_f8f6f4 v[152:155], v[4:11], v[44:51], 0, v221, v216 op_sel_hi:[0,0,0]
	v_mfma_scale_f32_16x16x128_f8f6f4 v[148:151], v[12:19], v[44:51], 0, v221, v216 op_sel_hi:[0,0,0]
	v_mfma_scale_f32_16x16x128_f8f6f4 v[136:139], v[4:11], v[36:43], 0, v221, v216 op_sel_hi:[0,0,0]
	v_mfma_scale_f32_16x16x128_f8f6f4 v[132:135], v[12:19], v[36:43], 0, v221, v216 op_sel_hi:[0,0,0]
	s_setprio 0
	s_barrier
	s_mov_b32 m0, s10
	v_lshl_add_u64 v[228:229], s[62:63], 0, v[196:197]
	s_add_u32 s86, s62, 0x8000
	ds_read_b128 v[36:39], v243 offset:16384
	ds_read_b128 v[40:43], v243 offset:17408
	ds_read_b128 v[44:47], v243 offset:18432
	ds_read_b128 v[48:51], v243 offset:19456
	ds_read_b128 v[52:55], v243 offset:20480
	ds_read_b128 v[56:59], v243 offset:21504
	ds_read_b128 v[60:63], v243 offset:22528
	ds_read_b128 v[64:67], v243 offset:23552
	global_load_lds_dwordx4 v[228:229], off
	v_lshl_add_u64 v[228:229], s[62:63], 0, v[0:1]
	s_mov_b32 m0, s11
	s_addc_u32 s87, s63, 0
	global_load_lds_dwordx4 v[228:229], off
	v_lshl_add_u64 v[228:229], s[86:87], 0, v[196:197]
	s_mov_b32 m0, s22
	s_nop 0
	global_load_lds_dwordx4 v[228:229], off
	v_lshl_add_u64 v[228:229], s[86:87], 0, v[0:1]
	s_mov_b32 m0, s25
	s_nop 0
	global_load_lds_dwordx4 v[228:229], off
	s_mov_b32 m0, s9
	s_nop 0
	global_load_lds_dwordx4 v198, s[66:67]
	s_mov_b32 m0, s28
	s_nop 0
	global_load_lds_dwordx4 v200, s[66:67]
	s_waitcnt vmcnt(8)
	s_waitcnt lgkmcnt(0)
	s_barrier
	s_setprio 1
	s_waitcnt lgkmcnt(0)
	v_mfma_scale_f32_16x16x128_f8f6f4 v[128:131], v[20:27], v[36:43], 0, v221, v216 op_sel_hi:[0,0,0]
	v_mfma_scale_f32_16x16x128_f8f6f4 v[124:127], v[28:35], v[36:43], 0, v221, v216 op_sel_hi:[0,0,0]
	v_mfma_scale_f32_16x16x128_f8f6f4 v[112:115], v[20:27], v[44:51], 0, v221, v216 op_sel_hi:[0,0,0]
	v_mfma_scale_f32_16x16x128_f8f6f4 v[108:111], v[28:35], v[44:51], 0, v221, v216 op_sel_hi:[0,0,0]
	v_mfma_scale_f32_16x16x128_f8f6f4 v[96:99], v[20:27], v[52:59], 0, v221, v216 op_sel_hi:[0,0,0]
	v_mfma_scale_f32_16x16x128_f8f6f4 v[92:95], v[28:35], v[52:59], 0, v221, v216 op_sel_hi:[0,0,0]
	v_mfma_scale_f32_16x16x128_f8f6f4 v[80:83], v[20:27], v[60:67], 0, v221, v216 op_sel_hi:[0,0,0]
	v_mfma_scale_f32_16x16x128_f8f6f4 v[76:79], v[28:35], v[60:67], 0, v221, v216 op_sel_hi:[0,0,0]
	s_setprio 0
	s_setprio 1
	v_mfma_scale_f32_16x16x128_f8f6f4 v[120:123], v[4:11], v[36:43], 0, v221, v216 op_sel_hi:[0,0,0]
	v_mfma_scale_f32_16x16x128_f8f6f4 v[116:119], v[12:19], v[36:43], 0, v221, v216 op_sel_hi:[0,0,0]
	v_mfma_scale_f32_16x16x128_f8f6f4 v[104:107], v[4:11], v[44:51], 0, v221, v216 op_sel_hi:[0,0,0]
	v_mfma_scale_f32_16x16x128_f8f6f4 v[100:103], v[12:19], v[44:51], 0, v221, v216 op_sel_hi:[0,0,0]
	v_mfma_scale_f32_16x16x128_f8f6f4 v[88:91], v[4:11], v[52:59], 0, v221, v216 op_sel_hi:[0,0,0]
	v_mfma_scale_f32_16x16x128_f8f6f4 v[84:87], v[12:19], v[52:59], 0, v221, v216 op_sel_hi:[0,0,0]
	v_mfma_scale_f32_16x16x128_f8f6f4 v[72:75], v[4:11], v[60:67], 0, v221, v216 op_sel_hi:[0,0,0]
	v_mfma_scale_f32_16x16x128_f8f6f4 v[68:71], v[12:19], v[60:67], 0, v221, v216 op_sel_hi:[0,0,0]
	s_setprio 0
	s_barrier
	s_branch .Lmid_po

; #define PG8_STAGEA(bufoff, gbase, h) do { if constexpr (GATHER) { PG8_STAGE(bufoff, gbase, vA[h]); } else { PG8_STAGE(bufoff, (gbase) + (h) * hstepA, voffA); } } while (0)
; #define PG8_LDA(dst, b, h) do { _Pragma("unroll") for (int m = 0; m < 4; ++m) _Pragma("unroll") for (int k = 0; k < 2; ++k) dst[m][k] = *(const LAS bf16x8*)(lds + PG8_SA(b, h) + aoff + m * 2048 + k * 1024); } while (0)
; #define PG8_MM(ai, bj, At, Bt) do { if constexpr (Epi::F8MMA) PG8_MMA8(ai, bj, At, Bt##8); else PG8_MMA(ai, bj, At, Bt); } while (0)
; #define PG8_WAIT_V(n) asm volatile("s_waitcnt vmcnt(" #n ")" ::: "memory")
; #define PG8_WAIT_L(n) asm volatile("s_waitcnt lgkmcnt(" #n ")" ::: "memory")
; #define PG8_BAR __builtin_amdgcn_s_barrier()
; #define PG8_SCHED __builtin_amdgcn_sched_barrier(0)
; template <class Epi, class Sched>
; __device__ __forceinline__ void gemm_phase(const int tid, LAS unsigned char* lds, const char* Abase, const int lda, const int ldb, const int K, const Sched& S, const Epi& E) {
;     ...
;             PG8_LDB(B0, 1, 0); PG8_LDB(B1, 1, 1); PG8_SCHED; PG8_LDA(At, 1, 0); PG8_STAGEA(PG8_SA(0, 1), a2, 1);
;             PG8_WAIT_V(8); PG8_WAIT_L(0); PG8_BAR; PG8_MM(0, 0, At, B0); PG8_MM(0, 1, At, B1); PG8_BAR; PG8_SCHED;
;             PG8_LDA(At, 1, 1); PG8_STAGE(PG8_SB(1, 0), b3, voffB); PG8_STAGE(PG8_SB(1, 1), b3 + hstepB, voffB); PG8_STAGEA(PG8_SA(1, 0), a3, 0);
;             PG8_WAIT_V(8); PG8_WAIT_L(0); PG8_BAR; PG8_MM(1, 0, At, B0); PG8_MM(1, 1, At, B1); PG8_BAR; PG8_SCHED;
;         }
.Lmid_po:
	s_add_i32 s86, 0, 0x18000
	s_add_i32 s87, 0, 0x1c000
	v_add_u32_e32 v16, s86, v199
	v_add_u32_e32 v32, s87, v199
	ds_read_b128 v[4:7], v16
	ds_read_b128 v[8:11], v16 offset:1024
	ds_read_b128 v[12:15], v16 offset:2048
	ds_read_b128 v[16:19], v16 offset:3072
	ds_read_b128 v[20:23], v32
	ds_read_b128 v[24:27], v32 offset:1024
	ds_read_b128 v[28:31], v32 offset:2048
	ds_read_b128 v[32:35], v32 offset:3072
	s_mov_b32 m0, s29
	v_lshl_add_u64 v[212:213], s[66:67], 0, v[212:213]
	ds_read_b128 v[36:39], v243 offset:32768
	ds_read_b128 v[40:43], v243 offset:33792
	ds_read_b128 v[44:47], v243 offset:34816
	ds_read_b128 v[48:51], v243 offset:35840
	ds_read_b128 v[52:55], v243 offset:36864
	ds_read_b128 v[56:59], v243 offset:37888
	ds_read_b128 v[60:63], v243 offset:38912
	ds_read_b128 v[64:67], v243 offset:39936
	global_load_lds_dwordx4 v[212:213], off
	v_lshl_add_u64 v[210:211], s[66:67], 0, v[210:211]
	s_mov_b32 m0, s68
	s_nop 0
	global_load_lds_dwordx4 v[210:211], off
	s_waitcnt vmcnt(8)
	s_waitcnt lgkmcnt(0)
	s_barrier
	s_setprio 1
	s_waitcnt lgkmcnt(0)
	v_mfma_scale_f32_16x16x128_f8f6f4 v[192:195], v[4:11], v[36:43], v[192:195], v221, v216 op_sel_hi:[0,0,0]
	v_mfma_scale_f32_16x16x128_f8f6f4 v[188:191], v[12:19], v[36:43], v[188:191], v221, v216 op_sel_hi:[0,0,0]
	v_mfma_scale_f32_16x16x128_f8f6f4 v[176:179], v[4:11], v[44:51], v[176:179], v221, v216 op_sel_hi:[0,0,0]
	v_mfma_scale_f32_16x16x128_f8f6f4 v[172:175], v[12:19], v[44:51], v[172:175], v221, v216 op_sel_hi:[0,0,0]
	v_mfma_scale_f32_16x16x128_f8f6f4 v[160:163], v[4:11], v[52:59], v[160:163], v221, v216 op_sel_hi:[0,0,0]
	v_mfma_scale_f32_16x16x128_f8f6f4 v[156:159], v[12:19], v[52:59], v[156:159], v221, v216 op_sel_hi:[0,0,0]
	v_mfma_scale_f32_16x16x128_f8f6f4 v[144:147], v[4:11], v[60:67], v[144:147], v221, v216 op_sel_hi:[0,0,0]
	v_mfma_scale_f32_16x16x128_f8f6f4 v[140:143], v[12:19], v[60:67], v[140:143], v221, v216 op_sel_hi:[0,0,0]
	s_setprio 0
	s_setprio 1
	v_mfma_scale_f32_16x16x128_f8f6f4 v[184:187], v[20:27], v[36:43], v[184:187], v221, v216 op_sel_hi:[0,0,0]
	v_mfma_scale_f32_16x16x128_f8f6f4 v[180:183], v[28:35], v[36:43], v[180:183], v221, v216 op_sel_hi:[0,0,0]
	v_mfma_scale_f32_16x16x128_f8f6f4 v[168:171], v[20:27], v[44:51], v[168:171], v221, v216 op_sel_hi:[0,0,0]
	v_mfma_scale_f32_16x16x128_f8f6f4 v[164:167], v[28:35], v[44:51], v[164:167], v221, v216 op_sel_hi:[0,0,0]
	v_mfma_scale_f32_16x16x128_f8f6f4 v[152:155], v[20:27], v[52:59], v[152:155], v221, v216 op_sel_hi:[0,0,0]
	v_mfma_scale_f32_16x16x128_f8f6f4 v[148:151], v[28:35], v[52:59], v[148:151], v221, v216 op_sel_hi:[0,0,0]
	v_mfma_scale_f32_16x16x128_f8f6f4 v[136:139], v[20:27], v[60:67], v[136:139], v221, v216 op_sel_hi:[0,0,0]
	v_mfma_scale_f32_16x16x128_f8f6f4 v[132:135], v[28:35], v[60:67], v[132:135], v221, v216 op_sel_hi:[0,0,0]
	s_setprio 0
	s_barrier
	s_add_i32 s66, s86, s8
	v_lshl_add_u64 v[210:211], s[64:65], 0, v[196:197]
	s_mov_b32 m0, s66
	ds_read_b128 v[36:39], v243 offset:49152
	ds_read_b128 v[40:43], v243 offset:50176
	ds_read_b128 v[44:47], v243 offset:51200
	ds_read_b128 v[48:51], v243 offset:52224
	ds_read_b128 v[52:55], v243 offset:53248
	ds_read_b128 v[56:59], v243 offset:54272
	ds_read_b128 v[60:63], v243 offset:55296
	ds_read_b128 v[64:67], v243 offset:56320
	global_load_lds_dwordx4 v[210:211], off
	s_add_i32 m0, s66, 0x2000
	s_add_u32 s62, s62, 0x8080
	v_lshl_add_u64 v[210:211], s[64:65], 0, v[0:1]
	s_addc_u32 s63, s63, 0
	s_add_i32 s64, s87, s8
	global_load_lds_dwordx4 v[210:211], off
	v_lshl_add_u64 v[210:211], s[62:63], 0, v[196:197]
	s_mov_b32 m0, s64
	s_nop 0
	global_load_lds_dwordx4 v[210:211], off
	v_lshl_add_u64 v[210:211], s[62:63], 0, v[0:1]
	s_add_i32 m0, s64, 0x2000
	s_nop 0
	global_load_lds_dwordx4 v[210:211], off
	s_mov_b32 m0, s69
	s_nop 0
	global_load_lds_dwordx4 v198, s[60:61]
	s_mov_b32 m0, s70
	s_nop 0
	global_load_lds_dwordx4 v200, s[60:61]
	s_waitcnt vmcnt(8)
	s_waitcnt lgkmcnt(0)
	s_barrier
	s_setprio 1
	s_waitcnt lgkmcnt(0)
	v_mfma_scale_f32_16x16x128_f8f6f4 v[128:131], v[4:11], v[36:43], v[128:131], v221, v216 op_sel_hi:[0,0,0]
	v_mfma_scale_f32_16x16x128_f8f6f4 v[124:127], v[12:19], v[36:43], v[124:127], v221, v216 op_sel_hi:[0,0,0]
	v_mfma_scale_f32_16x16x128_f8f6f4 v[112:115], v[4:11], v[44:51], v[112:115], v221, v216 op_sel_hi:[0,0,0]
	v_mfma_scale_f32_16x16x128_f8f6f4 v[108:111], v[12:19], v[44:51], v[108:111], v221, v216 op_sel_hi:[0,0,0]
	v_mfma_scale_f32_16x16x128_f8f6f4 v[96:99], v[4:11], v[52:59], v[96:99], v221, v216 op_sel_hi:[0,0,0]
	v_mfma_scale_f32_16x16x128_f8f6f4 v[92:95], v[12:19], v[52:59], v[92:95], v221, v216 op_sel_hi:[0,0,0]
	v_mfma_scale_f32_16x16x128_f8f6f4 v[80:83], v[4:11], v[60:67], v[80:83], v221, v216 op_sel_hi:[0,0,0]
	v_mfma_scale_f32_16x16x128_f8f6f4 v[76:79], v[12:19], v[60:67], v[76:79], v221, v216 op_sel_hi:[0,0,0]
	s_setprio 0
	s_setprio 1
	v_mfma_scale_f32_16x16x128_f8f6f4 v[120:123], v[20:27], v[36:43], v[120:123], v221, v216 op_sel_hi:[0,0,0]
	v_mfma_scale_f32_16x16x128_f8f6f4 v[116:119], v[28:35], v[36:43], v[116:119], v221, v216 op_sel_hi:[0,0,0]
	v_mfma_scale_f32_16x16x128_f8f6f4 v[104:107], v[20:27], v[44:51], v[104:107], v221, v216 op_sel_hi:[0,0,0]
	v_mfma_scale_f32_16x16x128_f8f6f4 v[100:103], v[28:35], v[44:51], v[100:103], v221, v216 op_sel_hi:[0,0,0]
	v_mfma_scale_f32_16x16x128_f8f6f4 v[88:91], v[20:27], v[52:59], v[88:91], v221, v216 op_sel_hi:[0,0,0]
	v_mfma_scale_f32_16x16x128_f8f6f4 v[84:87], v[28:35], v[52:59], v[84:87], v221, v216 op_sel_hi:[0,0,0]
	v_mfma_scale_f32_16x16x128_f8f6f4 v[72:75], v[20:27], v[60:67], v[72:75], v221, v216 op_sel_hi:[0,0,0]
	v_mfma_scale_f32_16x16x128_f8f6f4 v[68:71], v[28:35], v[60:67], v[68:71], v221, v216 op_sel_hi:[0,0,0]
	s_setprio 0
	s_barrier
	s_add_u32 s56, s56, 0x100
	s_addc_u32 s57, s57, 0
	s_cmp_ge_i32 s83, s5
	s_cbranch_scc1 .LBB0_1170
; #define PG8_STAGEA(bufoff, gbase, h) do { if constexpr (GATHER) { PG8_STAGE(bufoff, gbase, vA[h]); } else { PG8_STAGE(bufoff, (gbase) + (h) * hstepA, voffA); } } while (0)
; #define PG8_LDA(dst, b, h) do { _Pragma("unroll") for (int m = 0; m < 4; ++m) _Pragma("unroll") for (int k = 0; k < 2; ++k) dst[m][k] = *(const LAS bf16x8*)(lds + PG8_SA(b, h) + aoff + m * 2048 + k * 1024); } while (0)
; #define PG8_SCHED __builtin_amdgcn_sched_barrier(0)
; template <class Epi, class Sched>
; __device__ __forceinline__ void gemm_phase(const int tid, LAS unsigned char* lds, const char* Abase, const int lda, const int ldb, const int K, const Sched& S, const Epi& E) {
;     ...
;         for (int t = 0; t < nt; t += 2) {
;             const bool last = (t == nt - 2);
;             const char* a1 = cA + (size_t)(t + 1) * kstepA;
;             const char* a2 = last ? nA : cA + (size_t)(t + 2) * kstepA; const char* b2 = last ? nB : cB + (size_t)(t + 2) * kstep;
;             const char* a3 = a2 + kstepA; const char* b3 = b2 + kstep;
;             PG8_LDB(B0, 0, 0); PG8_LDB(B1, 0, 1); PG8_SCHED; PG8_LDA(At, 0, 0); PG8_STAGEA(PG8_SA(1, 1), a1, 1);
.LBB0_1167:
	v_add_u32_e32 v4, 0, v199
	v_add_u32_e32 v5, 0x10000, v4
	v_add_u32_e32 v16, 0x14000, v4
	ds_read_b128 v[20:23], v5
	ds_read_b128 v[24:27], v5 offset:1024
	ds_read_b128 v[28:31], v5 offset:2048
	ds_read_b128 v[32:35], v5 offset:3072
	ds_read_b128 v[4:7], v16
	ds_read_b128 v[8:11], v16 offset:1024
	ds_read_b128 v[12:15], v16 offset:2048
	ds_read_b128 v[16:19], v16 offset:3072
	s_cmp_eq_u32 s72, s83
	s_cselect_b64 s[62:63], -1, 0
	s_add_u32 s60, s40, s56
	s_addc_u32 s61, s41, s57
	s_add_u32 s60, s60, 0xffffff80
	s_addc_u32 s61, s61, -1
	s_add_i32 m0, s9, 0xc000
	s_add_i32 s64, s9, 0xe000
	s_cmp_lg_u32 s72, s83
	ds_read_b128 v[60:63], v243
	ds_read_b128 v[64:67], v243 offset:1024
	ds_read_b128 v[52:55], v243 offset:2048
	ds_read_b128 v[56:59], v243 offset:3072
	ds_read_b128 v[44:47], v243 offset:4096
	ds_read_b128 v[48:51], v243 offset:5120
	ds_read_b128 v[36:39], v243 offset:6144
	ds_read_b128 v[40:43], v243 offset:7168
	global_load_lds_dwordx4 v2, s[60:61]
	s_mov_b32 m0, s64
	s_nop 0
	global_load_lds_dwordx4 v202, s[60:61]
	s_cbranch_scc0 .LBB0_1165
	v_mov_b32_e32 v203, v3
	v_mov_b64_e32 v[210:211], v[202:203]
	v_mov_b64_e32 v[212:213], v[2:3]
	s_cmp_eq_u32 s83, 0
	s_cbranch_scc1 .Lpeel_po
	s_branch .LBB0_1166
